# phase 12: half of the workgroups run the attention-branch merge (memory-bound) before the GLU-gate GEMM (MFMA-bound) so the two overlap across workgroups; on top of v024
# baseline (speedup 1.0000x reference)
_Z4mega6Params:
	s_mov_b32 s98, 0
	v_writelane_b32 v253, s98, 61
	s_mov_b32 s98, 0
	v_writelane_b32 v253, s98, 60
	s_load_dwordx8 s[72:79], s[0:1], 0x100
	s_load_dwordx4 s[28:31], s[0:1], 0x120
	s_load_dword s34, s[0:1], 0x130
	s_mov_b32 s96, s2
	v_readfirstlane_b32 s2, v0
	v_cmp_gt_u32_e32 vcc, 64, v0
	s_nop 0
	v_writelane_b32 v254, s2, 0
	s_add_u32 s2, s0, 0x130
	s_addc_u32 s3, s1, 0
	v_writelane_b32 v254, s2, 1
	s_nop 1
	v_writelane_b32 v254, s3, 2
	s_and_saveexec_b64 s[4:5], vcc
	v_lshl_add_u32 v1, v0, 2, 0
	v_add_u32_e32 v1, 0x23f00, v1
	v_mov_b32_e32 v2, 0
	ds_write_b32 v1, v2
	s_or_b64 exec, exec, s[4:5]
	s_waitcnt lgkmcnt(0)
	s_add_u32 s2, s28, 0x4000
	s_load_dwordx16 s[8:23], s[0:1], 0x0
	s_addc_u32 s3, s29, 0
	v_writelane_b32 v254, s2, 3
	v_cmp_eq_u32_e32 vcc, 0, v0
	s_waitcnt lgkmcnt(0)
	v_writelane_b32 v254, s3, 4
	s_sub_i32 s2, s31, s30
	s_mov_b32 s3, 0
	v_writelane_b32 v254, s3, 5
	s_cmp_lt_i32 s2, 2
	s_mov_b32 s2, 0
	v_writelane_b32 v254, s2, 6
	s_barrier
	s_cbranch_scc1 .LBB0_7
	s_getreg_b32 s2, hwreg(HW_REG_XCC_ID, 0, 4)
	s_and_b32 s2, s2, 15
	v_writelane_b32 v254, s2, 5
	s_and_saveexec_b64 s[4:5], vcc
	s_cbranch_execz .LBB0_6
	s_mov_b64 s[6:7], exec
	v_mbcnt_lo_u32_b32 v1, s6, 0
	v_mbcnt_hi_u32_b32 v1, s7, v1
	v_cmp_eq_u32_e32 vcc, 0, v1
	s_and_b64 s[2:3], exec, vcc
	s_mov_b64 exec, s[2:3]
	s_cbranch_execz .LBB0_6
	v_readlane_b32 s2, v254, 5
	s_lshl_b32 s2, s2, 8
	s_bcnt1_i32_b64 s3, s[6:7]
	v_mov_b32_e32 v1, s2
	v_mov_b32_e32 v2, s3
	v_readlane_b32 s2, v254, 3
	v_readlane_b32 s3, v254, 4
	s_nop 4
	global_atomic_add v1, v2, s[2:3] offset:1024

.Lp12_gemm_entry:
	s_bitcmp1_b32 s96, 3
	s_cbranch_scc0 .Lp12_normal
	v_readlane_b32 s98, v253, 61
	s_cmp_eq_u32 s98, 0
	s_cbranch_scc1 .LBB0_1199
.Lp12_normal:
	s_cmpk_gt_i32 s96, 0xff
	v_readfirstlane_b32 s1, v0
	s_cbranch_scc1 .LBB0_1199
	s_add_u32 s4, s28, 0x3f400000
	v_lshlrev_b32_e32 v170, 4, v0
	s_waitcnt vmcnt(0)
	v_and_b32_e32 v2, 32, v0
	s_addc_u32 s5, s29, 0
	v_bfe_u32 v10, v0, 2, 4
	v_bitop3_b32 v8, v170, v2, 48 bitop3:0x6c
	v_and_b32_e32 v9, 64, v0
	v_lshrrev_b32_e32 v3, 3, v0
	s_add_u32 s3, s28, 0x7a00000
	v_or_b32_e32 v2, v8, v9
	v_and_or_b32 v3, v3, 48, v10
	v_or_b32_e32 v11, 0x2000, v170
	s_addc_u32 s33, s29, 0
	v_lshl_or_b32 v172, v3, 11, v2
	v_lshrrev_b32_e32 v3, 7, v11
	s_movk_i32 s0, 0x70
	s_ashr_i32 s39, s96, 31
	v_and_or_b32 v3, v3, s0, v10
	s_lshr_b32 s0, s39, 29
	s_add_i32 s0, s96, s0
	s_and_b32 s2, s0, -8
	s_lshr_b32 s26, s1, 6
	s_sub_i32 s2, s96, s2
	s_lshr_b32 s27, s1, 8
	s_lshl_b32 s35, s26, 10
	s_lshl_b32 s7, s2, 5
	s_ashr_i32 s0, s0, 3
	s_mul_i32 s6, s2, 33
	s_cmp_lt_i32 s2, 0
	s_cselect_b32 s2, s6, s7
	s_add_i32 s0, s2, s0
	s_ashr_i32 s2, s0, 31
	s_lshr_b32 s2, s2, 28
	s_add_i32 s2, s0, s2
	s_ashr_i32 s6, s2, 4
	s_and_b32 s2, s2, -16
	s_sub_i32 s2, s0, s2
	s_bfe_i32 s0, s2, 0x80000
	s_bfe_u32 s0, s0, 0x2000d
	s_add_i32 s7, s2, s0
	s_bfe_i32 s0, s7, 0x80000
	s_and_b32 s7, s7, 0xfc
	s_sub_i32 s2, s2, s7
	s_lshl_b32 s6, s6, 2
	s_sext_i32_i16 s0, s0
	s_sext_i32_i8 s2, s2
	s_lshr_b32 s0, s0, 2
	s_add_i32 s54, s6, s2
	s_ashr_i32 s55, s54, 31
	s_bfe_i64 s[6:7], s[0:1], 0x100000
	s_lshl_b64 s[14:15], s[54:55], 19
	s_lshl_b64 s[6:7], s[6:7], 19
	s_add_u32 s56, s3, s6
	v_mov_b32_e32 v171, 0
	s_addc_u32 s57, s33, s7
	s_add_i32 s55, s35, 0
	v_lshl_or_b32 v174, v3, 11, v2
	s_add_i32 m0, s55, 0x10000
	v_lshl_add_u64 v[2:3], s[56:57], 0, v[170:171]
	s_mov_b64 s[6:7], 0x2000
	global_load_lds_dwordx4 v170, s[56:57]
	v_lshl_add_u64 v[4:5], v[2:3], 0, s[6:7]
	s_add_i32 m0, s55, 0x12000
	s_mov_b64 s[10:11], 0x4000
	global_load_lds_dwordx4 v[4:5], off
	s_add_i32 m0, s55, 0x14000
	v_lshl_add_u64 v[4:5], v[2:3], 0, s[10:11]
	global_load_lds_dwordx4 v[4:5], off
	s_add_i32 m0, s55, 0x16000
	s_mov_b64 s[12:13], 0x6000
	s_add_u32 s58, s4, s14
	v_lshl_add_u64 v[4:5], v[2:3], 0, s[12:13]
	s_addc_u32 s59, s5, s15
	s_add_i32 s60, s55, 0x2000
	global_load_lds_dwordx4 v[4:5], off
	s_mov_b32 m0, s55
	s_add_u32 s14, s58, 0x40000
	global_load_lds_dwordx4 v172, s[58:59]
	s_mov_b32 m0, s60
	s_addc_u32 s15, s59, 0
	s_add_i32 s61, s55, 0x4000
	global_load_lds_dwordx4 v174, s[58:59]
	s_mov_b32 m0, s61
	s_add_i32 s62, s55, 0x6000
	global_load_lds_dwordx4 v172, s[14:15]
	s_mov_b32 m0, s62
	v_mov_b32_e32 v173, v171
	global_load_lds_dwordx4 v174, s[14:15]
	v_mov_b32_e32 v175, v171
	s_cmp_eq_u32 s27, 1
	s_mov_b32 s63, 0
	v_lshl_add_u64 v[4:5], s[58:59], 0, v[172:173]
	s_cselect_b64 s[14:15], -1, 0
	s_cmp_lg_u32 s27, 1
	v_lshl_add_u64 v[6:7], s[58:59], 0, v[174:175]
	s_cbranch_scc1 .LBB0_1182
	s_barrier

.LBB0_1199:
	s_bitcmp1_b32 s96, 3
	s_cbranch_scc0 .Lp12_merge
	v_readlane_b32 s98, v253, 61
	s_cmp_lg_u32 s98, 0
	s_cbranch_scc1 .LBB0_1207

.LBB0_1206:
	s_or_b64 exec, exec, s[10:11]
	v_readlane_b32 s98, v254, 60
	s_bitcmp1_b32 s98, 3
	s_cbranch_scc0 .Lp12_done
	v_readlane_b32 s98, v253, 61
	s_cmp_lg_u32 s98, 0
	s_cbranch_scc1 .Lp12_done
	s_mov_b32 s98, 1
	v_writelane_b32 v253, s98, 61
	v_readlane_b32 s96, v254, 60
	s_branch .Lp12_gemm_entry
.Lp12_done:
.LBB0_1207:
	s_cmp_gt_i32 s31, 13
	s_cselect_b64 s[0:1], -1, 0
	s_and_b64 s[2:3], s[8:9], s[0:1]
	s_andn2_b64 vcc, exec, s[2:3]
	s_cbranch_vccnz .LBB0_1257
	s_waitcnt vmcnt(0)
	v_cmp_eq_u32_e32 vcc, 0, v0
	s_waitcnt vmcnt(0)
	s_barrier
	s_and_saveexec_b64 s[4:5], vcc
	s_cbranch_execz .LBB0_1256
	v_readlane_b32 s2, v254, 6
	s_waitcnt vmcnt(0) expcnt(0) lgkmcnt(0)
	s_nop 0
	v_mov_b32_e32 v1, s2
	ds_read_b32 v3, v1
	ds_read_b32 v1, v1 offset:4
	s_waitcnt lgkmcnt(1)
	v_cmp_ne_u32_e32 vcc, 0, v3
	s_cbranch_vccnz .LBB0_1224
	v_readlane_b32 s6, v254, 1
	v_readlane_b32 s7, v254, 2
	s_load_dwordx2 s[2:3], s[6:7], 0x4
	s_add_u32 s6, s28, 0x4200
	s_addc_u32 s7, s29, 0
	s_add_u32 s8, s28, 0x4400
	s_addc_u32 s9, s29, 0
	s_add_u32 s10, s28, 0x4500
	s_addc_u32 s11, s29, 0
	s_add_u32 s12, s28, 0x4600
	s_addc_u32 s13, s29, 0
	s_add_u32 s14, s28, 0x4700
	s_addc_u32 s15, s29, 0
	s_add_u32 s16, s28, 0x4800
	s_addc_u32 s17, s29, 0
	s_add_u32 s18, s28, 0x4900
	s_addc_u32 s19, s29, 0
	s_add_u32 s20, s28, 0x4a00
	s_addc_u32 s21, s29, 0
	s_add_u32 s22, s28, 0x4b00
	s_addc_u32 s23, s29, 0
	s_add_u32 s24, s28, 0x4c00
	s_addc_u32 s25, s29, 0
	s_add_u32 s36, s28, 0x4d00
	s_addc_u32 s37, s29, 0
	s_add_u32 s38, s28, 0x4e00
	s_addc_u32 s39, s29, 0
	s_add_u32 s40, s28, 0x4f00
	s_addc_u32 s41, s29, 0
	s_add_u32 s42, s28, 0x5000
	s_addc_u32 s43, s29, 0
	s_add_u32 s44, s28, 0x5100
	s_addc_u32 s45, s29, 0
	s_add_u32 s50, s28, 0x5200
	s_addc_u32 s51, s29, 0
	s_waitcnt lgkmcnt(0)
	s_mul_i32 s2, s2, s34
	s_add_u32 s52, s28, 0x5300
	s_mul_i32 s2, s2, s3
	s_addc_u32 s53, s29, 0
	s_mov_b32 s3, 1
	v_mov_b32_e32 v17, 0
	s_branch .LBB0_1212
